# static s_setprio: slow-path (refine) waves prio 3, K2 loader waves prio 2
# speedup vs baseline: 1.0046x; 1.0025x over previous
.LBB1_10:
	s_setprio 2
	s_load_dwordx4 s[4:7], s[0:1], 0x0
	s_lshl_b32 s0, s14, 2
	s_mov_b32 s13, 0
	s_sub_i32 s3, s0, 32
	s_lshl_b64 s[0:1], s[12:13], 18
	s_waitcnt lgkmcnt(0)
	s_add_u32 s4, s4, s0
	s_addc_u32 s5, s5, s1
	s_add_u32 s6, s6, s0
	s_addc_u32 s7, s7, s1
	s_lshl_b32 s0, s2, 9
	s_lshl_b32 s8, s2, 7
	s_and_b32 s0, s0, 0xe00
	v_lshrrev_b32_e32 v1, 4, v1
	s_add_u32 s2, s4, s0
	v_or_b32_e32 v2, s3, v1
	v_bitop3_b32 v1, s3, v0, v1 bitop3:0x36
	s_addc_u32 s3, s5, 0
	v_lshlrev_b32_e32 v3, 4, v0
	s_add_u32 s0, s6, s0
	v_and_b32_e32 v3, 0xf0, v3
	s_addc_u32 s1, s7, 0
	v_lshl_or_b32 v128, v2, 12, v3
	global_load_dwordx4 v[72:75], v128, s[2:3] nt
	s_add_u32 s10, s2, 0x10000
	global_load_dwordx4 v[84:87], v128, s[0:1] nt
	s_addc_u32 s11, s3, 0
	global_load_dwordx4 v[64:67], v128, s[10:11] nt
	s_add_u32 s10, s0, 0x10000
	s_addc_u32 s11, s1, 0
	global_load_dwordx4 v[92:95], v128, s[10:11] nt
	s_add_u32 s10, s2, 0x20000
	s_addc_u32 s11, s3, 0
	global_load_dwordx4 v[68:71], v128, s[10:11] nt
	s_add_u32 s10, s0, 0x20000
	s_addc_u32 s11, s1, 0
	global_load_dwordx4 v[100:103], v128, s[10:11] nt
	s_add_u32 s10, s2, 0x30000
	s_addc_u32 s11, s3, 0
	global_load_dwordx4 v[76:79], v128, s[10:11] nt
	s_add_u32 s10, s0, 0x30000
	s_addc_u32 s11, s1, 0
	global_load_dwordx4 v[108:111], v128, s[10:11] nt
	s_add_u32 s10, s2, 0x40000
	s_addc_u32 s11, s3, 0
	global_load_dwordx4 v[80:83], v128, s[10:11] nt
	s_add_u32 s10, s0, 0x40000
	s_addc_u32 s11, s1, 0
	global_load_dwordx4 v[112:115], v128, s[10:11] nt
	s_add_u32 s10, s2, 0x50000
	s_addc_u32 s11, s3, 0
	global_load_dwordx4 v[88:91], v128, s[10:11] nt
	s_add_u32 s10, s0, 0x50000
	s_addc_u32 s11, s1, 0
	global_load_dwordx4 v[116:119], v128, s[10:11] nt
	s_add_u32 s10, s2, 0x60000
	s_addc_u32 s11, s3, 0
	global_load_dwordx4 v[96:99], v128, s[10:11] nt
	s_add_u32 s10, s0, 0x60000
	s_addc_u32 s11, s1, 0
	global_load_dwordx4 v[120:123], v128, s[10:11] nt
	s_add_u32 s10, s2, 0x70000
	s_addc_u32 s11, s3, 0
	global_load_dwordx4 v[104:107], v128, s[10:11] nt
	s_add_u32 s10, s0, 0x70000
	s_addc_u32 s11, s1, 0
	global_load_dwordx4 v[124:127], v128, s[10:11] nt
	s_add_u32 s10, s2, 0x100
	s_addc_u32 s11, s3, 0
	s_add_u32 s12, s0, 0x100
	v_lshlrev_b32_e32 v1, 3, v1
	v_lshlrev_b32_e32 v0, 3, v0
	s_addc_u32 s13, s1, 0
	v_and_b32_e32 v129, 0x70, v1
	v_and_b32_e32 v130, 8, v0
	v_lshlrev_b32_e32 v131, 7, v2
	global_load_dwordx4 v[0:3], v128, s[10:11] nt
	s_add_u32 s10, s2, 0x10100
	global_load_dwordx4 v[4:7], v128, s[12:13] nt
	s_addc_u32 s11, s3, 0
	global_load_dwordx4 v[8:11], v128, s[10:11] nt
	s_add_u32 s10, s0, 0x10100
	s_addc_u32 s11, s1, 0
	global_load_dwordx4 v[12:15], v128, s[10:11] nt
	s_add_u32 s10, s2, 0x20100
	s_addc_u32 s11, s3, 0
	global_load_dwordx4 v[16:19], v128, s[10:11] nt
	s_add_u32 s10, s0, 0x20100
	s_addc_u32 s11, s1, 0
	global_load_dwordx4 v[20:23], v128, s[10:11] nt
	s_add_u32 s10, s2, 0x30100
	s_addc_u32 s11, s3, 0
	global_load_dwordx4 v[24:27], v128, s[10:11] nt
	s_add_u32 s10, s0, 0x30100
	s_addc_u32 s11, s1, 0
	global_load_dwordx4 v[28:31], v128, s[10:11] nt
	s_add_u32 s10, s2, 0x40100
	s_addc_u32 s11, s3, 0
	global_load_dwordx4 v[32:35], v128, s[10:11] nt
	s_add_u32 s10, s0, 0x40100
	s_addc_u32 s11, s1, 0
	global_load_dwordx4 v[36:39], v128, s[10:11] nt
	s_add_u32 s10, s2, 0x50100
	s_addc_u32 s11, s3, 0
	global_load_dwordx4 v[40:43], v128, s[10:11] nt
	s_add_u32 s10, s0, 0x50100
	s_addc_u32 s11, s1, 0
	global_load_dwordx4 v[44:47], v128, s[10:11] nt
	s_add_u32 s10, s2, 0x60100
	s_addc_u32 s11, s3, 0
	global_load_dwordx4 v[48:51], v128, s[10:11] nt
	s_add_u32 s10, s0, 0x60100
	s_addc_u32 s11, s1, 0
	s_add_u32 s2, s2, 0x70100
	global_load_dwordx4 v[52:55], v128, s[10:11] nt
	s_addc_u32 s3, s3, 0
	global_load_dwordx4 v[56:59], v128, s[2:3] nt
	s_add_u32 s0, s0, 0x70100
	s_addc_u32 s1, s1, 0
	global_load_dwordx4 v[60:63], v128, s[0:1] nt
	s_waitcnt vmcnt(16)
	v_or3_b32 v129, v129, v131, v130
	v_pk_add_f32 v[74:75], v[74:75], v[86:87]
	v_pk_add_f32 v[72:73], v[72:73], v[84:85]
	v_pk_add_f32 v[66:67], v[66:67], v[94:95]
	v_pk_add_f32 v[64:65], v[64:65], v[92:93]
	v_add_u32_e32 v130, 0x20000, v129
	v_cvt_pk_f16_f32 v75, v74, v75
	v_cvt_pk_f16_f32 v74, v72, v73
	v_cvt_pk_f16_f32 v67, v66, v67
	v_cvt_pk_f16_f32 v66, v64, v65
	ds_write2st64_b64 v130, v[74:75], v[66:67] offset1:4
	v_pk_add_f32 v[64:65], v[70:71], v[102:103]
	v_pk_add_f32 v[66:67], v[68:69], v[100:101]
	v_cvt_pk_f16_f32 v65, v64, v65
	v_cvt_pk_f16_f32 v64, v66, v67
	v_pk_add_f32 v[66:67], v[78:79], v[110:111]
	v_pk_add_f32 v[68:69], v[76:77], v[108:109]
	v_cvt_pk_f16_f32 v67, v66, v67
	v_cvt_pk_f16_f32 v66, v68, v69
	ds_write2st64_b64 v130, v[64:65], v[66:67] offset0:8 offset1:12
	v_pk_add_f32 v[64:65], v[82:83], v[114:115]
	v_pk_add_f32 v[66:67], v[80:81], v[112:113]
	v_cvt_pk_f16_f32 v65, v64, v65
	v_cvt_pk_f16_f32 v64, v66, v67
	v_pk_add_f32 v[66:67], v[90:91], v[118:119]
	v_pk_add_f32 v[68:69], v[88:89], v[116:117]
	v_cvt_pk_f16_f32 v67, v66, v67
	v_cvt_pk_f16_f32 v66, v68, v69
	ds_write2st64_b64 v130, v[64:65], v[66:67] offset0:16 offset1:20
	v_pk_add_f32 v[64:65], v[98:99], v[122:123]
	v_pk_add_f32 v[66:67], v[96:97], v[120:121]
	v_cvt_pk_f16_f32 v65, v64, v65
	v_cvt_pk_f16_f32 v64, v66, v67
	v_pk_add_f32 v[66:67], v[106:107], v[126:127]
	v_pk_add_f32 v[68:69], v[104:105], v[124:125]
	v_cvt_pk_f16_f32 v67, v66, v67
	v_cvt_pk_f16_f32 v66, v68, v69
	ds_write2st64_b64 v130, v[64:65], v[66:67] offset0:24 offset1:28
	s_waitcnt lgkmcnt(0)
	s_barrier
	s_addk_i32 s8, 0x80
	s_mov_b32 s9, -2

.Lrg_slow:
	s_setprio 3
	s_getpc_b64 s[4:5]
	s_and_b32 s4, s4, -16
	v_lshlrev_b32_e32 v2, 4, v1
	global_load_dwordx4 v[100:103], v2, s[4:5] offset:0
	global_load_dwordx4 v[104:107], v2, s[4:5] offset:1024
	global_load_dwordx4 v[108:111], v2, s[4:5] offset:2048
	global_load_dwordx4 v[112:115], v2, s[4:5] offset:3072
	s_add_u32 s4, s4, 0x1000
	s_addc_u32 s5, s5, 0
	global_load_dwordx4 v[116:119], v2, s[4:5] offset:0
	global_load_dwordx4 v[120:123], v2, s[4:5] offset:1024
	global_load_dwordx4 v[124:127], v2, s[4:5] offset:2048
	global_load_dwordx4 v[128:131], v2, s[4:5] offset:3072
	s_add_u32 s4, s4, 0x1000
	s_addc_u32 s5, s5, 0
	s_mov_b32 s3, s24
	s_mov_b32 s33, s27
	v_mov_b32_e32 v26, v1
	v_cmp_gt_u32_e64 s[10:11], 64, v0
	v_mov_b32_e32 v2, s50
	v_mov_b32_e32 v3, s51
	v_mov_b32_e32 v4, s54
	v_mov_b32_e32 v5, s55
	v_mov_b32_e32 v1, 0
	v_cmp_eq_u32_e32 vcc, 0, v0
	s_and_saveexec_b64 s[6:7], vcc
	ds_write_b128 v1, v[2:5] offset:16400
